# v25
# speedup vs baseline: 1.1069x; 1.0156x over previous
.LBB3_8:
	s_or_b64 exec, exec, s[0:1]
	v_readlane_b32 s0, v0, 8
	v_readlane_b32 s1, v0, 2
	v_readlane_b32 s78, v0, 0
	v_readlane_b32 s4, v0, 4
	v_readlane_b32 s5, v0, 6
	s_sub_i32 s33, s1, s78
	s_sub_i32 s96, s4, s1
	s_sub_i32 s97, s5, s4
	s_sub_i32 s75, s0, s5
	s_max_i32 s1, s33, s96
	v_mov_b32_e32 v0, s97
	v_mov_b32_e32 v1, s75
	s_sub_i32 s23, s0, s78
	v_max3_i32 v166, s1, v0, v1
	s_add_i32 s0, s23, -1
	s_cmpk_gt_u32 s0, 0x7f
	s_cselect_b64 s[0:1], -1, 0
	v_cmp_lt_i32_e32 vcc, 64, v166
	s_or_b64 s[4:5], s[0:1], vcc
	s_mov_b64 s[0:1], -1
	s_and_b64 vcc, exec, s[4:5]
	v_lshlrev_b32_e32 v165, 3, v189
	v_ashrrev_i32_e32 v190, 2, v189
	v_ashrrev_i32_e32 v191, 5, v189
	v_and_b32_e32 v192, 31, v189
	s_cbranch_vccz .LBB3_86
	v_cmp_lt_i32_e32 vcc, v183, v184
	v_and_b32_e32 v169, 3, v189
	v_ashrrev_i32_e32 v168, 5, v189
	v_cndmask_b32_e32 v0, v182, v183, vcc
	v_lshlrev_b32_e32 v170, 2, v0
	v_and_b32_e32 v0, 0xffffffe0, v189
	v_cmp_lt_i32_e32 vcc, v185, v184
	v_add_u32_e32 v174, s88, v0
	v_ashrrev_i32_e32 v164, 2, v189
	v_cndmask_b32_e32 v0, v182, v185, vcc
	v_cmp_lt_i32_e32 vcc, v186, v184
	v_lshlrev_b32_e32 v175, 2, v0
	v_and_b32_e32 v167, 31, v189
	v_cndmask_b32_e32 v0, v182, v186, vcc
	v_cmp_lt_i32_e32 vcc, v187, v184
	v_lshl_add_u32 v172, v169, 3, s88
	v_lshlrev_b32_e32 v193, 2, v0
	v_cndmask_b32_e32 v0, v182, v187, vcc
	v_lshlrev_b32_e32 v196, 7, v168
	v_cmp_gt_u32_e64 s[0:1], 4, v189
	v_cmp_gt_u32_e64 s[4:5], 32, v189
	s_mov_b32 s24, 0
	v_lshlrev_b32_e32 v171, 2, v167
	v_lshl_add_u32 v173, v164, 5, v172
	v_lshlrev_b32_e32 v194, 2, v0
	v_lshl_add_u32 v195, v168, 2, s88
	v_add_u32_e32 v197, 0x100, v196
	v_add_u32_e32 v198, 0x200, v196
	v_add_u32_e32 v199, 0x300, v196
	v_add_u32_e32 v200, s88, v165
	s_branch .LBB3_11

.LBB3_111:
	s_or_b64 exec, exec, s[0:1]
	v_ashrrev_i32_e32 v167, 3, v189
	v_mov_b32_e32 v0, s87
	v_and_b32_e32 v169, -2, v167
	v_lshl_add_u32 v1, v167, 2, s87
	s_waitcnt vmcnt(0)
	v_lshl_add_u32 v2, v169, 2, s87
	ds_read_b32 v0, v0
	ds_read_b32 v168, v2
	ds_read2_b32 v[160:161], v1 offset1:1
	v_subrev_u32_e32 v194, s78, v167
	s_add_i32 s79, s23, -1
	v_and_b32_e32 v193, 7, v189
	s_waitcnt lgkmcnt(0)
	v_add_u32_e32 v0, v194, v0
	v_min_i32_e32 v1, s79, v0
	v_add_u32_e32 v2, 8, v0
	v_add_u32_e32 v3, 16, v0
	v_add_u32_e32 v4, 24, v0
	v_min_i32_e32 v2, s79, v2
	v_min_i32_e32 v3, s79, v3
	v_min_i32_e32 v4, s79, v4
	v_lshl_add_u32 v1, v1, 2, s90
	v_lshl_add_u32 v2, v2, 2, s90
	v_lshl_add_u32 v3, v3, 2, s90
	v_lshl_add_u32 v4, v4, 2, s90
	ds_read_b32 v1, v1
	ds_read_b32 v2, v2
	ds_read_b32 v3, v3
	ds_read_b32 v4, v4
	s_waitcnt lgkmcnt(3)
	v_lshl_or_b32 v176, v1, 3, v193
	v_lshl_add_u64 v[20:21], v[176:177], 4, s[72:73]
	global_load_dwordx4 v[20:23], v[20:21], off
	s_waitcnt lgkmcnt(2)
	v_lshl_or_b32 v176, v2, 3, v193
	v_lshl_add_u64 v[16:17], v[176:177], 4, s[72:73]
	global_load_dwordx4 v[16:19], v[16:17], off
	s_waitcnt lgkmcnt(1)
	v_lshl_or_b32 v176, v3, 3, v193
	v_lshl_add_u64 v[28:29], v[176:177], 4, s[72:73]
	global_load_dwordx4 v[28:31], v[28:29], off
	s_waitcnt lgkmcnt(0)
	v_lshl_or_b32 v176, v4, 3, v193
	v_lshl_add_u64 v[24:25], v[176:177], 4, s[72:73]
	global_load_dwordx4 v[24:27], v[24:25], off
.LBB3_119:
	s_add_i32 s0, s78, s33
	v_add_u32_e32 v162, s0, v194
	v_min_i32_e32 v163, s79, v162
	v_add_u32_e32 v164, 8, v162
	v_add_u32_e32 v170, 16, v162
	v_add_u32_e32 v171, 24, v162
	v_min_i32_e32 v164, s79, v164
	v_min_i32_e32 v170, s79, v170
	v_min_i32_e32 v171, s79, v171
	v_lshl_add_u32 v163, v163, 2, s90
	v_lshl_add_u32 v164, v164, 2, s90
	v_lshl_add_u32 v170, v170, 2, s90
	v_lshl_add_u32 v171, v171, 2, s90
	ds_read_b32 v163, v163
	ds_read_b32 v164, v164
	ds_read_b32 v170, v170
	ds_read_b32 v171, v171
	s_waitcnt lgkmcnt(3)
	v_lshl_or_b32 v176, v163, 3, v193
	v_lshl_add_u64 v[4:5], v[176:177], 4, s[72:73]
	global_load_dwordx4 v[4:7], v[4:5], off
	s_waitcnt lgkmcnt(2)
	v_lshl_or_b32 v176, v164, 3, v193
	v_lshl_add_u64 v[0:1], v[176:177], 4, s[72:73]
	global_load_dwordx4 v[0:3], v[0:1], off
	s_waitcnt lgkmcnt(1)
	v_lshl_or_b32 v176, v170, 3, v193
	v_lshl_add_u64 v[12:13], v[176:177], 4, s[72:73]
	global_load_dwordx4 v[12:15], v[12:13], off
	s_waitcnt lgkmcnt(0)
	v_lshl_or_b32 v176, v171, 3, v193
	v_lshl_add_u64 v[8:9], v[176:177], 4, s[72:73]
	global_load_dwordx4 v[8:11], v[8:9], off

.LBB3_129:
	v_mov_b32_e32 v162, v227
	v_subrev_u32_e32 v164, s78, v160
	v_lshl_add_u32 v171, v193, 2, s88
	v_lshl_add_u32 v237, v164, 5, v171
	ds_read_b32 v173, v237 offset:32
	ds_read_b32 v174, v237 offset:64
	ds_read_b32 v175, v237 offset:96
	ds_read_b32 v176, v237 offset:128
	ds_read_b32 v195, v237 offset:160
	ds_read_b32 v196, v237 offset:192
	ds_read_b32 v197, v237 offset:224
	ds_read_b32 v198, v237 offset:256
	ds_read_b32 v199, v237 offset:288
	ds_read_b32 v200, v237 offset:320
	ds_read_b32 v201, v237 offset:352
	ds_read_b32 v202, v237 offset:384
	ds_read_b32 v203, v237 offset:416
	ds_read_b32 v204, v237 offset:448
	ds_read_b32 v205, v237 offset:480
	ds_read_b32 v206, v237 offset:512
	ds_read_b32 v207, v237 offset:544
	ds_read_b32 v208, v237 offset:576
	ds_read_b32 v209, v237 offset:608
	ds_read_b32 v210, v237 offset:640
	ds_read_b32 v211, v237 offset:672
	ds_read_b32 v170, v237 offset:704
	ds_read_b32 v163, v237 offset:736
	v_sub_u32_e32 v166, v161, v160
	v_cmp_lt_i32_e64 s[44:45], 0, v166
	v_mov_b32_e32 v172, 0xff800000
	s_and_saveexec_b64 s[0:1], s[44:45]
	s_cbranch_execz .LBB3_131
	v_min_i32_e32 v161, 0x7f, v164
	v_lshl_add_u32 v161, v161, 5, v171
	ds_read_b32 v161, v161
	s_waitcnt lgkmcnt(0)
	v_add_f32_e32 v161, v162, v161
	v_mul_f32_e32 v172, 0x3e4ccccd, v161
	v_cmp_le_f32_e32 vcc, 0, v161
	s_nop 1
	v_cndmask_b32_e32 v172, v172, v161, vcc

.LBB3_196:
	s_or_b64 exec, exec, s[4:5]
	v_lshlrev_b32_e32 v197, 7, v167
	v_add_u32_e32 v160, s88, v197
	v_lshlrev_b32_e32 v164, 4, v193
	v_add_u32_e32 v198, v160, v164
	s_waitcnt vmcnt(0)
	ds_write_b128 v198, v[20:23]
	ds_write_b128 v198, v[16:19] offset:1024
	ds_write_b128 v198, v[28:31] offset:2048
	ds_write_b128 v198, v[24:27] offset:3072
	s_add_i32 s0, s78, s33
	s_add_i32 s0, s0, s96
	v_add_u32_e32 v160, s0, v194
	v_min_i32_e32 v168, s79, v160
	v_add_u32_e32 v169, 8, v160
	v_add_u32_e32 v170, 16, v160
	v_add_u32_e32 v171, 24, v160
	v_min_i32_e32 v169, s79, v169
	v_min_i32_e32 v170, s79, v170
	v_min_i32_e32 v171, s79, v171
	v_lshl_add_u32 v168, v168, 2, s90
	v_lshl_add_u32 v169, v169, 2, s90
	v_lshl_add_u32 v170, v170, 2, s90
	v_lshl_add_u32 v171, v171, 2, s90
	ds_read_b32 v168, v168
	ds_read_b32 v169, v169
	ds_read_b32 v170, v170
	ds_read_b32 v171, v171
	s_waitcnt lgkmcnt(3)
	v_lshl_or_b32 v176, v168, 3, v193
	v_lshl_add_u64 v[16:17], v[176:177], 4, s[72:73]
	global_load_dwordx4 v[16:19], v[16:17], off
	s_waitcnt lgkmcnt(2)
	v_lshl_or_b32 v176, v169, 3, v193
	v_lshl_add_u64 v[24:25], v[176:177], 4, s[72:73]
	global_load_dwordx4 v[24:27], v[24:25], off
	s_waitcnt lgkmcnt(1)
	v_lshl_or_b32 v176, v170, 3, v193
	v_lshl_add_u64 v[20:21], v[176:177], 4, s[72:73]
	global_load_dwordx4 v[20:23], v[20:21], off
	s_waitcnt lgkmcnt(0)
	v_lshl_or_b32 v176, v171, 3, v193
	v_lshl_add_u64 v[28:29], v[176:177], 4, s[72:73]
	global_load_dwordx4 v[28:31], v[28:29], off

.LBB3_207:
	v_lshrrev_b32_e32 v176, 3, v195
	v_lshlrev_b32_e32 v204, 7, v193
	v_or_b32_e32 v176, s86, v176
	v_lshl_add_u32 v203, v203, 3, v204
	v_mul_lo_u32 v176, v176, s69
	v_add_u32_e32 v203, v203, v176
	s_nop 0
	v_cvt_pk_f16_f32 v163, v162, v163
	v_cvt_pk_f16_f32 v162, v160, v161
	v_cvt_pk_f16_f32 v161, v166, v167
	v_cvt_pk_f16_f32 v160, v164, v165
	v_cvt_pk_f16_f32 v175, v174, v175
	v_cvt_pk_f16_f32 v174, v172, v173
	v_cvt_pk_f16_f32 v171, v170, v171
	v_cvt_pk_f16_f32 v170, v168, v169
	ds_write2_b64 v203, v[162:163], v[160:161] offset0:8 offset1:12
	v_mov_b32_e32 v160, s87
	ds_write2_b64 v203, v[174:175], v[170:171] offset1:4
	ds_write_b128 v198, v[4:7]
	ds_write_b128 v198, v[0:3] offset:1024
	ds_write_b128 v198, v[12:15] offset:2048
	ds_write_b128 v198, v[8:11] offset:3072
	s_add_i32 s0, s78, s33
	s_add_i32 s0, s0, s96
	s_add_i32 s0, s0, s97
	v_add_u32_e32 v160, s0, v194
	v_min_i32_e32 v161, s79, v160
	v_add_u32_e32 v162, 8, v160
	v_add_u32_e32 v163, 16, v160
	v_add_u32_e32 v166, 24, v160
	v_min_i32_e32 v162, s79, v162
	v_min_i32_e32 v163, s79, v163
	v_min_i32_e32 v166, s79, v166
	v_lshl_add_u32 v161, v161, 2, s90
	v_lshl_add_u32 v162, v162, 2, s90
	v_lshl_add_u32 v163, v163, 2, s90
	v_lshl_add_u32 v166, v166, 2, s90
	ds_read_b32 v161, v161
	ds_read_b32 v162, v162
	ds_read_b32 v163, v163
	ds_read_b32 v166, v166
	s_waitcnt lgkmcnt(3)
	v_lshl_or_b32 v176, v161, 3, v193
	v_lshl_add_u64 v[4:5], v[176:177], 4, s[72:73]
	global_load_dwordx4 v[4:7], v[4:5], off
	s_waitcnt lgkmcnt(2)
	v_lshl_or_b32 v176, v162, 3, v193
	v_lshl_add_u64 v[0:1], v[176:177], 4, s[72:73]
	global_load_dwordx4 v[0:3], v[0:1], off
	s_waitcnt lgkmcnt(1)
	v_lshl_or_b32 v176, v163, 3, v193
	v_lshl_add_u64 v[12:13], v[176:177], 4, s[72:73]
	global_load_dwordx4 v[12:15], v[12:13], off
	s_waitcnt lgkmcnt(0)
	v_lshl_or_b32 v176, v166, 3, v193
	v_lshl_add_u64 v[8:9], v[176:177], 4, s[72:73]
	global_load_dwordx4 v[8:11], v[8:9], off

.LBB3_222:
	v_lshlrev_b32_e32 v0, 4, v168
	v_add_u32_e32 v165, 0xca00, v0
	v_mad_u32_u24 v166, v167, s69, v0
	v_add_u32_e32 v12, s66, v165
	s_waitcnt lgkmcnt(0)
	s_barrier
	ds_read_b128 v[16:19], v12
	ds_read_b128 v[20:23], v12 offset:32
	ds_read_b128 v[24:27], v12 offset:64
	ds_read_b128 v[28:31], v12 offset:96
	v_add_u32_e32 v169, s95, v166
	ds_read_b128 v[160:163], v169
	ds_read_b128 v[170:173], v169 offset:32
	s_waitcnt lgkmcnt(1)
	v_mfma_f32_32x32x16_f16 v[16:31], v[96:99], v[160:163], v[16:31]
	ds_read_b128 v[0:3], v12 offset:128
	ds_read_b128 v[4:7], v12 offset:160
	ds_read_b128 v[8:11], v12 offset:192
	ds_read_b128 v[12:15], v12 offset:224
	v_lshlrev_b32_e32 v168, 3, v168
	v_mad_u32_u24 v174, v167, s69, v168
	v_add_u32_e32 v167, s95, v174
	s_mov_b32 s8, 0xc34f
	s_waitcnt lgkmcnt(4)
	v_mfma_f32_32x32x16_f16 v[16:31], v[100:103], v[170:173], v[16:31]
	s_waitcnt lgkmcnt(0)
	v_mfma_f32_32x32x16_f16 v[0:15], v[112:115], v[160:163], v[0:15]
	ds_read_b128 v[160:163], v169 offset:64
	ds_read_b128 v[190:193], v169 offset:96
	s_waitcnt lgkmcnt(1)
	v_mfma_f32_32x32x16_f16 v[16:31], v[104:107], v[160:163], v[16:31]
	v_mfma_f32_32x32x16_f16 v[0:15], v[116:119], v[170:173], v[0:15]
	s_waitcnt lgkmcnt(0)
	v_mfma_f32_32x32x16_f16 v[16:31], v[108:111], v[190:193], v[16:31]
	v_mfma_f32_32x32x16_f16 v[0:15], v[120:123], v[160:163], v[0:15]
	s_nop 10
	v_max_f32_e32 v168, 0, v17
	v_max_f32_e32 v17, 0, v18
	v_max_f32_e32 v18, 0, v19
	v_max_f32_e32 v16, 0, v16
	v_max_f32_e32 v20, 0, v20
	v_max_f32_e32 v21, 0, v21
	v_cvt_pk_f16_f32 v17, v17, v18
	v_max_f32_e32 v18, 0, v22
	v_max_f32_e32 v19, 0, v23
	v_mfma_f32_32x32x16_f16 v[0:15], v[124:127], v[190:193], v[0:15]
	v_cvt_pk_f16_f32 v16, v16, v168
	v_cvt_pk_f16_f32 v19, v18, v19
	v_cvt_pk_f16_f32 v18, v20, v21
	ds_write2_b64 v167, v[16:17], v[18:19] offset1:2
	v_max_f32_e32 v18, 0, v25
	v_max_f32_e32 v17, 0, v26
	v_max_f32_e32 v19, 0, v27
	v_max_f32_e32 v16, 0, v24
	v_cvt_pk_f16_f32 v17, v17, v19
	v_cvt_pk_f16_f32 v16, v16, v18
	v_max_f32_e32 v20, 0, v29
	v_max_f32_e32 v18, 0, v28
	v_max_f32_e32 v19, 0, v30
	v_max_f32_e32 v21, 0, v31
	v_cvt_pk_f16_f32 v19, v19, v21
	v_cvt_pk_f16_f32 v18, v18, v20
	ds_write2_b64 v167, v[16:17], v[18:19] offset0:4 offset1:6
	v_max_f32_e32 v16, 0, v1
	v_max_f32_e32 v1, v2, v2
	v_max_f32_e32 v1, 0, v1
	v_max_f32_e32 v2, 0, v3
	v_cvt_pk_f16_f32 v1, v1, v2
	v_max_f32_e32 v2, v4, v4
	v_max_f32_e32 v4, 0, v5
	v_max_f32_e32 v0, 0, v0
	v_max_f32_e32 v2, 0, v2
	v_max_f32_e32 v3, 0, v6
	v_max_f32_e32 v5, 0, v7
	v_cvt_pk_f16_f32 v0, v0, v16
	v_cvt_pk_f16_f32 v3, v3, v5
	v_cvt_pk_f16_f32 v2, v2, v4
	ds_write2_b64 v167, v[0:1], v[2:3] offset0:8 offset1:10
	v_max_f32_e32 v2, 0, v9
	v_max_f32_e32 v1, 0, v10
	v_max_f32_e32 v3, 0, v11
	v_max_f32_e32 v0, 0, v8
	v_cvt_pk_f16_f32 v1, v1, v3
	v_cvt_pk_f16_f32 v0, v0, v2
	v_max_f32_e32 v4, 0, v13
	v_max_f32_e32 v2, 0, v12
	v_max_f32_e32 v3, 0, v14
	v_max_f32_e32 v5, 0, v15
	v_cvt_pk_f16_f32 v3, v3, v5
	v_cvt_pk_f16_f32 v2, v2, v4
	ds_write2_b64 v167, v[0:1], v[2:3] offset0:12 offset1:14
	v_add_u32_e32 v12, s64, v165
	ds_read_b128 v[16:19], v12
	ds_read_b128 v[20:23], v12 offset:32
	ds_read_b128 v[24:27], v12 offset:64
	ds_read_b128 v[28:31], v12 offset:96
	v_add_u32_e32 v165, s98, v166
	ds_read_b128 v[160:163], v165
	ds_read_b128 v[166:169], v165 offset:32
	ds_read_b128 v[0:3], v12 offset:128
	ds_read_b128 v[4:7], v12 offset:160
	ds_read_b128 v[8:11], v12 offset:192
	ds_read_b128 v[12:15], v12 offset:224
	s_waitcnt lgkmcnt(5)
	v_mfma_f32_32x32x16_f16 v[16:31], v[128:131], v[160:163], v[16:31]
	s_waitcnt lgkmcnt(0)
	v_mfma_f32_32x32x16_f16 v[0:15], v[144:147], v[160:163], v[0:15]
	v_mfma_f32_32x32x16_f16 v[16:31], v[132:135], v[166:169], v[16:31]
	v_mfma_f32_32x32x16_f16 v[0:15], v[148:151], v[166:169], v[0:15]
	ds_read_b128 v[160:163], v165 offset:64
	ds_read_b128 v[166:169], v165 offset:96
	s_waitcnt lgkmcnt(1)
	v_mfma_f32_32x32x16_f16 v[16:31], v[136:139], v[160:163], v[16:31]
	s_waitcnt lgkmcnt(0)
	v_mfma_f32_32x32x16_f16 v[16:31], v[140:143], v[166:169], v[16:31]
	v_mfma_f32_32x32x16_f16 v[0:15], v[152:155], v[160:163], v[0:15]
	s_nop 10
	v_max_f32_e32 v161, 0, v17
	v_max_f32_e32 v17, v18, v18
	v_max_f32_e32 v17, 0, v17
	v_max_f32_e32 v18, 0, v19
	v_cvt_pk_f16_f32 v17, v17, v18
	v_max_f32_e32 v18, v20, v20
	v_max_f32_e32 v20, 0, v21
	v_mfma_f32_32x32x16_f16 v[0:15], v[156:159], v[166:169], v[0:15]
	v_max_f32_e32 v16, 0, v16
	v_max_f32_e32 v18, 0, v18
	v_max_f32_e32 v19, 0, v22
	v_max_f32_e32 v21, 0, v23
	v_add_u32_e32 v160, s98, v174
	v_cvt_pk_f16_f32 v16, v16, v161
	v_cvt_pk_f16_f32 v19, v19, v21
	v_cvt_pk_f16_f32 v18, v18, v20
	ds_write2_b64 v160, v[16:17], v[18:19] offset1:2
	v_max_f32_e32 v18, 0, v25
	v_max_f32_e32 v17, 0, v26
	v_max_f32_e32 v19, 0, v27
	v_max_f32_e32 v16, 0, v24
	v_cvt_pk_f16_f32 v17, v17, v19
	v_cvt_pk_f16_f32 v16, v16, v18
	v_max_f32_e32 v20, 0, v29
	v_max_f32_e32 v18, 0, v28
	v_max_f32_e32 v19, 0, v30
	v_max_f32_e32 v21, 0, v31
	v_cvt_pk_f16_f32 v19, v19, v21
	v_cvt_pk_f16_f32 v18, v18, v20
	ds_write2_b64 v160, v[16:17], v[18:19] offset0:4 offset1:6
	v_max_f32_e32 v16, 0, v1
	v_max_f32_e32 v1, v2, v2
	v_max_f32_e32 v1, 0, v1
	v_max_f32_e32 v2, 0, v3
	v_cvt_pk_f16_f32 v1, v1, v2
	v_max_f32_e32 v2, v4, v4
	v_max_f32_e32 v4, 0, v5
	v_max_f32_e32 v0, 0, v0
	v_max_f32_e32 v2, 0, v2
	v_max_f32_e32 v3, 0, v6
	v_max_f32_e32 v5, 0, v7
	v_cvt_pk_f16_f32 v0, v0, v16
	v_cvt_pk_f16_f32 v3, v3, v5
	v_cvt_pk_f16_f32 v2, v2, v4
	ds_write2_b64 v160, v[0:1], v[2:3] offset0:8 offset1:10
	v_max_f32_e32 v2, 0, v9
	v_max_f32_e32 v1, 0, v10
	v_max_f32_e32 v3, 0, v11
	v_max_f32_e32 v0, 0, v8
	v_cvt_pk_f16_f32 v1, v1, v3
	v_cvt_pk_f16_f32 v0, v0, v2
	v_max_f32_e32 v4, 0, v13
	v_max_f32_e32 v2, 0, v12
	v_max_f32_e32 v3, 0, v14
	v_max_f32_e32 v5, 0, v15
	v_cvt_pk_f16_f32 v3, v3, v5
	v_cvt_pk_f16_f32 v2, v2, v4
	v_mad_u32_u24 v12, v195, s69, v196
	ds_write2_b64 v160, v[0:1], v[2:3] offset0:12 offset1:14
	s_waitcnt lgkmcnt(0)
	s_barrier
	v_mul_u32_u24_e32 v16, 0x410, v195
	v_add_u32_e32 v16, v196, v16
	ds_read_b128 v[8:11], v16
	ds_read_b128 v[12:15], v16 offset:16640
	ds_read_b128 v[20:23], v16 offset:64
	ds_read_b128 v[24:27], v16 offset:16704
	ds_read_b128 v[28:31], v16 offset:128
	ds_read_b128 v[160:163], v16 offset:16768
	ds_read_b128 v[164:167], v16 offset:192
	ds_read_b128 v[168:171], v16 offset:16832
	s_waitcnt lgkmcnt(7)
	v_mfma_f32_16x16x32_f16 v[0:3], v[32:35], v[8:11], 0
	ds_read_b128 v[8:11], v16 offset:256
	s_waitcnt lgkmcnt(7)
	v_mfma_f32_16x16x32_f16 v[4:7], v[32:35], v[12:15], 0
	ds_read_b128 v[12:15], v16 offset:16896
	s_waitcnt lgkmcnt(7)
	v_mfma_f32_16x16x32_f16 v[0:3], v[36:39], v[20:23], v[0:3]
	ds_read_b128 v[20:23], v16 offset:320
	s_waitcnt lgkmcnt(7)
	v_mfma_f32_16x16x32_f16 v[4:7], v[36:39], v[24:27], v[4:7]
	ds_read_b128 v[24:27], v16 offset:16960
	s_waitcnt lgkmcnt(7)
	v_mfma_f32_16x16x32_f16 v[0:3], v[40:43], v[28:31], v[0:3]
	ds_read_b128 v[28:31], v16 offset:384
	s_waitcnt lgkmcnt(7)
	v_mfma_f32_16x16x32_f16 v[4:7], v[40:43], v[160:163], v[4:7]
	ds_read_b128 v[160:163], v16 offset:17024
	s_waitcnt lgkmcnt(7)
	v_mfma_f32_16x16x32_f16 v[0:3], v[44:47], v[164:167], v[0:3]
	ds_read_b128 v[164:167], v16 offset:448
	s_waitcnt lgkmcnt(7)
	v_mfma_f32_16x16x32_f16 v[4:7], v[44:47], v[168:171], v[4:7]
	ds_read_b128 v[168:171], v16 offset:17088
	s_waitcnt lgkmcnt(7)
	v_mfma_f32_16x16x32_f16 v[0:3], v[56:59], v[8:11], v[0:3]
	ds_read_b128 v[8:11], v16 offset:512
	s_waitcnt lgkmcnt(7)
	v_mfma_f32_16x16x32_f16 v[4:7], v[56:59], v[12:15], v[4:7]
	ds_read_b128 v[12:15], v16 offset:17152
	s_waitcnt lgkmcnt(7)
	v_mfma_f32_16x16x32_f16 v[0:3], v[48:51], v[20:23], v[0:3]
	ds_read_b128 v[20:23], v16 offset:576
	s_waitcnt lgkmcnt(7)
	v_mfma_f32_16x16x32_f16 v[4:7], v[48:51], v[24:27], v[4:7]
	ds_read_b128 v[24:27], v16 offset:17216
	s_waitcnt lgkmcnt(7)
	v_mfma_f32_16x16x32_f16 v[0:3], v[52:55], v[28:31], v[0:3]
	ds_read_b128 v[28:31], v16 offset:640
	s_waitcnt lgkmcnt(7)
	v_mfma_f32_16x16x32_f16 v[4:7], v[52:55], v[160:163], v[4:7]
	ds_read_b128 v[160:163], v16 offset:17280
	s_waitcnt lgkmcnt(7)
	v_mfma_f32_16x16x32_f16 v[0:3], v[76:79], v[164:167], v[0:3]
	ds_read_b128 v[164:167], v16 offset:704
	s_waitcnt lgkmcnt(7)
	v_mfma_f32_16x16x32_f16 v[4:7], v[76:79], v[168:171], v[4:7]
	ds_read_b128 v[168:171], v16 offset:17344
	s_waitcnt lgkmcnt(7)
	v_mfma_f32_16x16x32_f16 v[0:3], v[60:63], v[8:11], v[0:3]
	ds_read_b128 v[8:11], v16 offset:768
	s_waitcnt lgkmcnt(7)
	v_mfma_f32_16x16x32_f16 v[4:7], v[60:63], v[12:15], v[4:7]
	ds_read_b128 v[12:15], v16 offset:17408
	s_waitcnt lgkmcnt(7)
	v_mfma_f32_16x16x32_f16 v[0:3], v[64:67], v[20:23], v[0:3]
	ds_read_b128 v[20:23], v16 offset:832
	s_waitcnt lgkmcnt(7)
	v_mfma_f32_16x16x32_f16 v[4:7], v[64:67], v[24:27], v[4:7]
	ds_read_b128 v[24:27], v16 offset:17472
	s_waitcnt lgkmcnt(7)
	v_mfma_f32_16x16x32_f16 v[0:3], v[68:71], v[28:31], v[0:3]
	ds_read_b128 v[28:31], v16 offset:896
	s_waitcnt lgkmcnt(7)
	v_mfma_f32_16x16x32_f16 v[4:7], v[68:71], v[160:163], v[4:7]
	ds_read_b128 v[160:163], v16 offset:17536
	s_waitcnt lgkmcnt(7)
	v_mfma_f32_16x16x32_f16 v[0:3], v[72:75], v[164:167], v[0:3]
	ds_read_b128 v[164:167], v16 offset:960
	s_waitcnt lgkmcnt(7)
	v_mfma_f32_16x16x32_f16 v[4:7], v[72:75], v[168:171], v[4:7]
	ds_read_b128 v[168:171], v16 offset:17600
	s_waitcnt lgkmcnt(7)
	v_mfma_f32_16x16x32_f16 v[0:3], v[80:83], v[8:11], v[0:3]
	s_waitcnt lgkmcnt(6)
	v_mfma_f32_16x16x32_f16 v[4:7], v[80:83], v[12:15], v[4:7]
	s_waitcnt lgkmcnt(5)
	v_mfma_f32_16x16x32_f16 v[0:3], v[84:87], v[20:23], v[0:3]
	s_waitcnt lgkmcnt(4)
	v_mfma_f32_16x16x32_f16 v[4:7], v[84:87], v[24:27], v[4:7]
	s_waitcnt lgkmcnt(3)
	v_mfma_f32_16x16x32_f16 v[0:3], v[88:91], v[28:31], v[0:3]
	s_waitcnt lgkmcnt(2)
	v_mfma_f32_16x16x32_f16 v[4:7], v[88:91], v[160:163], v[4:7]
	s_waitcnt lgkmcnt(1)
	v_mfma_f32_16x16x32_f16 v[0:3], v[92:95], v[164:167], v[0:3]
	s_waitcnt lgkmcnt(0)
	v_mfma_f32_16x16x32_f16 v[4:7], v[92:95], v[168:171], v[4:7]
	v_lshrrev_b32_e32 v17, 4, v189
	v_lshlrev_b32_e32 v17, 3, v17
	s_lshl_b32 s0, s3, 1
	v_add_u32_e32 v18, s74, v195
	v_lshl_add_u32 v17, v18, 7, v17
	v_add_u32_e32 v17, s0, v17
	v_readlane_b32 s4, v226, 0
	v_readlane_b32 s5, v226, 1
	s_mov_b32 s1, 0xc350
	v_add_u32_e32 v19, 16, v18
	v_lshlrev_b32_e32 v28, 2, v195
	s_nop 1
	v_cvt_pk_f16_f32 v20, v0, v1
	v_cvt_pk_f16_f32 v21, v2, v3
	v_cvt_pk_f16_f32 v22, v4, v5
	v_cvt_pk_f16_f32 v23, v6, v7
	v_cmp_gt_i32_e32 vcc, s1, v18
	v_cmp_gt_i32_e64 s[8:9], s1, v19
	v_mul_f32_e32 v24, v228, v0
	v_mul_f32_e32 v25, v232, v0
	v_mul_f32_e32 v26, v228, v4
	v_mul_f32_e32 v27, v232, v4
	v_fmac_f32_e32 v24, v229, v1
	v_fmac_f32_e32 v25, v233, v1
	v_fmac_f32_e32 v26, v229, v5
	v_fmac_f32_e32 v27, v233, v5
	v_fmac_f32_e32 v24, v230, v2
	v_fmac_f32_e32 v25, v234, v2
	v_fmac_f32_e32 v26, v230, v6
	v_fmac_f32_e32 v27, v234, v6
	v_fmac_f32_e32 v24, v231, v3
	v_fmac_f32_e32 v25, v235, v3
	v_fmac_f32_e32 v26, v231, v7
	v_fmac_f32_e32 v27, v235, v7
	s_mov_b64 exec, vcc
	global_store_dwordx2 v17, v[20:21], s[4:5]
	s_mov_b64 exec, s[8:9]
	global_store_dwordx2 v17, v[22:23], s[4:5] offset:2048
	s_mov_b64 exec, -1
	v_mov_b32_e32 v12, v24
	v_mov_b32_e32 v13, v25
	v_mov_b32_e32 v14, v26
	v_mov_b32_e32 v15, v27
	s_nop 1
	v_permlane32_swap_b32_e32 v24, v12
	v_permlane32_swap_b32_e32 v25, v13
	v_permlane32_swap_b32_e32 v26, v14
	v_permlane32_swap_b32_e32 v27, v15
	v_add_f32_e32 v24, v24, v12
	v_add_f32_e32 v25, v25, v13
	v_add_f32_e32 v26, v26, v14
	v_add_f32_e32 v27, v27, v15
	ds_swizzle_b32 v12, v24 offset:0x401f
	ds_swizzle_b32 v13, v25 offset:0x401f
	ds_swizzle_b32 v14, v26 offset:0x401f
	ds_swizzle_b32 v15, v27 offset:0x401f
	s_waitcnt lgkmcnt(0)
	v_add_f32_e32 v24, v24, v12
	v_add_f32_e32 v25, v25, v13
	v_add_f32_e32 v26, v26, v14
	v_add_f32_e32 v27, v27, v15
	s_lshl_b32 s0, s3, 4
	s_add_i32 s0, s0, 0xd3c0
	v_lshl_add_u32 v28, v195, 2, s0
	s_mov_b64 exec, 0xffff
	ds_write_b32 v28, v24
	ds_write_b32 v28, v26 offset:64
	ds_write_b32 v28, v25 offset:128
	ds_write_b32 v28, v27 offset:192
	s_mov_b64 exec, -1
	v_add_u32_e32 v1, s65, v189
	v_cmp_gt_i32_e32 vcc, 32, v1
	s_waitcnt lgkmcnt(0)
	s_barrier
	s_and_saveexec_b64 s[0:1], vcc
	s_cbranch_execz .LBB3_5
	v_add_u32_e32 v0, s74, v1
	s_mov_b32 s4, 0xc350
	v_lshlrev_b32_e32 v1, 2, v1
	v_cmp_gt_i32_e32 vcc, s4, v0
	v_add_u32_e32 v2, 0xd000, v1
	s_and_saveexec_b64 s[4:5], vcc
	s_cbranch_execz .LBB3_4
	v_add_u32_e32 v8, 0xd3c0, v1
	v_add_u32_e32 v9, 0xd440, v1
	ds_read2st64_b32 v[4:5], v8 offset1:1
	ds_read2st64_b32 v[10:11], v8 offset0:2 offset1:3
	ds_read2st64_b32 v[12:13], v9 offset1:1
	ds_read2st64_b32 v[14:15], v9 offset0:2 offset1:3
	v_ashrrev_i32_e32 v1, 31, v0
	v_readlane_b32 s8, v226, 0
	v_lshlrev_b64 v[0:1], 2, v[0:1]
	v_readlane_b32 s10, v226, 2
	v_readlane_b32 s11, v226, 3
	v_lshl_add_u64 v[6:7], s[76:77], 0, v[0:1]
	v_readlane_b32 s9, v226, 1
	v_lshl_add_u64 v[0:1], s[10:11], 0, v[0:1]
	s_waitcnt lgkmcnt(0)
	v_add_f32_e32 v5, v4, v5
	v_add_f32_e32 v10, v10, v11
	v_add_f32_e32 v4, v12, v13
	v_add_f32_e32 v12, v14, v15
	v_add_f32_e32 v5, v5, v10
	v_add_f32_e32 v4, v4, v12
	global_store_dword v[0:1], v5, off
	global_store_dword v[6:7], v4, off
	s_branch .LBB3_4

	.amdhsa_kernel _Z8k_layer1PKiS0_PKfS2_PK15HIP_vector_typeIjLj4EEPKDv8_DF16_S9_S2_S2_S2_PDF16_PfSB_
		.amdhsa_group_segment_fixed_size 55232
		.amdhsa_private_segment_fixed_size 0
		.amdhsa_kernarg_size 360
		.amdhsa_user_sgpr_count 2
		.amdhsa_user_sgpr_dispatch_ptr 0
		.amdhsa_user_sgpr_queue_ptr 0
		.amdhsa_user_sgpr_kernarg_segment_ptr 1
		.amdhsa_user_sgpr_dispatch_id 0
		.amdhsa_user_sgpr_kernarg_preload_length 0
		.amdhsa_user_sgpr_kernarg_preload_offset 0
		.amdhsa_user_sgpr_private_segment_size 0
		.amdhsa_uses_dynamic_stack 0
		.amdhsa_enable_private_segment 0
		.amdhsa_system_sgpr_workgroup_id_x 1
		.amdhsa_system_sgpr_workgroup_id_y 0
		.amdhsa_system_sgpr_workgroup_id_z 0
		.amdhsa_system_sgpr_workgroup_info 0
		.amdhsa_system_vgpr_workitem_id 0
		.amdhsa_next_free_vgpr 238
		.amdhsa_next_free_sgpr 100
		.amdhsa_accum_offset 240
		.amdhsa_reserve_vcc 1
		.amdhsa_float_round_mode_32 0
		.amdhsa_float_round_mode_16_64 0
		.amdhsa_float_denorm_mode_32 3
		.amdhsa_float_denorm_mode_16_64 3
		.amdhsa_dx10_clamp 1
		.amdhsa_ieee_mode 1
		.amdhsa_fp16_overflow 0
		.amdhsa_tg_split 0
		.amdhsa_exception_fp_ieee_invalid_op 0
		.amdhsa_exception_fp_denorm_src 0
		.amdhsa_exception_fp_ieee_div_zero 0
		.amdhsa_exception_fp_ieee_overflow 0
		.amdhsa_exception_fp_ieee_underflow 0
		.amdhsa_exception_fp_ieee_inexact 0
		.amdhsa_exception_int_div_zero 0
	.end_amdhsa_kernel

amdhsa.kernels:
  - .agpr_count:     0
    .args:
      - .actual_access:  read_only
        .address_space:  global
        .offset:         0
        .size:           8
        .value_kind:     global_buffer
      - .actual_access:  read_only
        .address_space:  global
        .offset:         8
        .size:           8
        .value_kind:     global_buffer
      - .actual_access:  read_only
        .address_space:  global
        .offset:         16
        .size:           8
        .value_kind:     global_buffer
      - .actual_access:  read_only
        .address_space:  global
        .offset:         24
        .size:           8
        .value_kind:     global_buffer
      - .actual_access:  read_only
        .address_space:  global
        .offset:         32
        .size:           8
        .value_kind:     global_buffer
      - .actual_access:  write_only
        .address_space:  global
        .offset:         40
        .size:           8
        .value_kind:     global_buffer
      - .actual_access:  write_only
        .address_space:  global
        .offset:         48
        .size:           8
        .value_kind:     global_buffer
      - .actual_access:  write_only
        .address_space:  global
        .offset:         56
        .size:           8
        .value_kind:     global_buffer
      - .actual_access:  write_only
        .address_space:  global
        .offset:         64
        .size:           8
        .value_kind:     global_buffer
    .group_segment_fixed_size: 1024
    .kernarg_segment_align: 8
    .kernarg_segment_size: 72
    .language:       OpenCL C
    .language_version:
      - 2
      - 0
    .max_flat_workgroup_size: 512
    .name:           _Z11k_hist_prepPKiPKfS2_S2_S2_PiPfPDF16_S5_
    .private_segment_fixed_size: 0
    .sgpr_count:     20
    .sgpr_spill_count: 0
    .symbol:         _Z11k_hist_prepPKiPKfS2_S2_S2_PiPfPDF16_S5_.kd
    .uniform_work_group_size: 1
    .uses_dynamic_stack: false
    .vgpr_count:     42
    .vgpr_spill_count: 0
    .wavefront_size: 64
  - .agpr_count:     0
    .args:
      - .actual_access:  read_only
        .address_space:  global
        .offset:         0
        .size:           8
        .value_kind:     global_buffer
      - .actual_access:  read_only
        .address_space:  global
        .offset:         8
        .size:           8
        .value_kind:     global_buffer
      - .actual_access:  write_only
        .address_space:  global
        .offset:         16
        .size:           8
        .value_kind:     global_buffer
      - .actual_access:  write_only
        .address_space:  global
        .offset:         24
        .size:           8
        .value_kind:     global_buffer
      - .actual_access:  read_only
        .address_space:  global
        .offset:         32
        .size:           8
        .value_kind:     global_buffer
      - .actual_access:  read_only
        .address_space:  global
        .offset:         40
        .size:           8
        .value_kind:     global_buffer
      - .actual_access:  write_only
        .address_space:  global
        .offset:         48
        .size:           8
        .value_kind:     global_buffer
      - .actual_access:  write_only
        .address_space:  global
        .offset:         56
        .size:           8
        .value_kind:     global_buffer
      - .actual_access:  write_only
        .address_space:  global
        .offset:         64
        .size:           8
        .value_kind:     global_buffer
    .group_segment_fixed_size: 9344
    .kernarg_segment_align: 8
    .kernarg_segment_size: 72
    .language:       OpenCL C
    .language_version:
      - 2
      - 0
    .max_flat_workgroup_size: 512
    .name:           _Z14k_scatter_nodePKiS0_PjPiPKfS4_PfS5_PDF16_
    .private_segment_fixed_size: 0
    .sgpr_count:     106
    .sgpr_spill_count: 10
    .symbol:         _Z14k_scatter_nodePKiS0_PjPiPKfS4_PfS5_PDF16_.kd
    .uniform_work_group_size: 1
    .uses_dynamic_stack: false
    .vgpr_count:     118
    .vgpr_spill_count: 0
    .wavefront_size: 64
  - .agpr_count:     0
    .args:
      - .actual_access:  read_only
        .address_space:  global
        .offset:         0
        .size:           8
        .value_kind:     global_buffer
      - .actual_access:  read_only
        .address_space:  global
        .offset:         8
        .size:           8
        .value_kind:     global_buffer
      - .actual_access:  write_only
        .address_space:  global
        .offset:         16
        .size:           8
        .value_kind:     global_buffer
      - .actual_access:  write_only
        .address_space:  global
        .offset:         24
        .size:           8
        .value_kind:     global_buffer
    .group_segment_fixed_size: 3072
    .kernarg_segment_align: 8
    .kernarg_segment_size: 32
    .language:       OpenCL C
    .language_version:
      - 2
      - 0
    .max_flat_workgroup_size: 1024
    .name:           _Z5k_csrPKjPKiPiS3_
    .private_segment_fixed_size: 0
    .sgpr_count:     34
    .sgpr_spill_count: 0
    .symbol:         _Z5k_csrPKjPKiPiS3_.kd
    .uniform_work_group_size: 1
    .uses_dynamic_stack: false
    .vgpr_count:     18
    .vgpr_spill_count: 0
    .wavefront_size: 64
  - .agpr_count:     0
    .args:
      - .actual_access:  read_only
        .address_space:  global
        .offset:         0
        .size:           8
        .value_kind:     global_buffer
      - .actual_access:  read_only
        .address_space:  global
        .offset:         8
        .size:           8
        .value_kind:     global_buffer
      - .actual_access:  read_only
        .address_space:  global
        .offset:         16
        .size:           8
        .value_kind:     global_buffer
      - .actual_access:  read_only
        .address_space:  global
        .offset:         24
        .size:           8
        .value_kind:     global_buffer
      - .actual_access:  read_only
        .address_space:  global
        .offset:         32
        .size:           8
        .value_kind:     global_buffer
      - .actual_access:  read_only
        .address_space:  global
        .offset:         40
        .size:           8
        .value_kind:     global_buffer
      - .actual_access:  read_only
        .address_space:  global
        .offset:         48
        .size:           8
        .value_kind:     global_buffer
      - .actual_access:  read_only
        .address_space:  global
        .offset:         56
        .size:           8
        .value_kind:     global_buffer
      - .actual_access:  read_only
        .address_space:  global
        .offset:         64
        .size:           8
        .value_kind:     global_buffer
      - .actual_access:  read_only
        .address_space:  global
        .offset:         72
        .size:           8
        .value_kind:     global_buffer
      - .actual_access:  write_only
        .address_space:  global
        .offset:         80
        .size:           8
        .value_kind:     global_buffer
      - .actual_access:  write_only
        .address_space:  global
        .offset:         88
        .size:           8
        .value_kind:     global_buffer
      - .actual_access:  write_only
        .address_space:  global
        .offset:         96
        .size:           8
        .value_kind:     global_buffer
      - .offset:         104
        .size:           4
        .value_kind:     hidden_block_count_x
      - .offset:         108
        .size:           4
        .value_kind:     hidden_block_count_y
      - .offset:         112
        .size:           4
        .value_kind:     hidden_block_count_z
      - .offset:         116
        .size:           2
        .value_kind:     hidden_group_size_x
      - .offset:         118
        .size:           2
        .value_kind:     hidden_group_size_y
      - .offset:         120
        .size:           2
        .value_kind:     hidden_group_size_z
      - .offset:         122
        .size:           2
        .value_kind:     hidden_remainder_x
      - .offset:         124
        .size:           2
        .value_kind:     hidden_remainder_y
      - .offset:         126
        .size:           2
        .value_kind:     hidden_remainder_z
      - .offset:         144
        .size:           8
        .value_kind:     hidden_global_offset_x
      - .offset:         152
        .size:           8
        .value_kind:     hidden_global_offset_y
      - .offset:         160
        .size:           8
        .value_kind:     hidden_global_offset_z
      - .offset:         168
        .size:           2
        .value_kind:     hidden_grid_dims
    .group_segment_fixed_size: 55232
    .kernarg_segment_align: 8
    .kernarg_segment_size: 360
    .language:       OpenCL C
    .language_version:
      - 2
      - 0
    .max_flat_workgroup_size: 256
    .name:           _Z8k_layer1PKiS0_PKfS2_PK15HIP_vector_typeIjLj4EEPKDv8_DF16_S9_S2_S2_S2_PDF16_PfSB_
    .private_segment_fixed_size: 0
    .sgpr_count:     106
    .sgpr_spill_count: 7
    .symbol:         _Z8k_layer1PKiS0_PKfS2_PK15HIP_vector_typeIjLj4EEPKDv8_DF16_S9_S2_S2_S2_PDF16_PfSB_.kd
    .uniform_work_group_size: 1
    .uses_dynamic_stack: false
    .vgpr_count:     238
    .vgpr_spill_count: 0
    .wavefront_size: 64
  - .agpr_count:     0
    .args:
      - .actual_access:  read_only
        .address_space:  global
        .offset:         0
        .size:           8
        .value_kind:     global_buffer
      - .actual_access:  read_only
        .address_space:  global
        .offset:         8
        .size:           8
        .value_kind:     global_buffer
      - .actual_access:  read_only
        .address_space:  global
        .offset:         16
        .size:           8
        .value_kind:     global_buffer
      - .actual_access:  read_only
        .address_space:  global
        .offset:         24
        .size:           8
        .value_kind:     global_buffer
      - .actual_access:  read_only
        .address_space:  global
        .offset:         32
        .size:           8
        .value_kind:     global_buffer
      - .actual_access:  read_only
        .address_space:  global
        .offset:         40
        .size:           8
        .value_kind:     global_buffer
      - .actual_access:  write_only
        .address_space:  global
        .offset:         48
        .size:           8
        .value_kind:     global_buffer
    .group_segment_fixed_size: 0
    .kernarg_segment_align: 8
    .kernarg_segment_size: 56
    .language:       OpenCL C
    .language_version:
      - 2
      - 0
    .max_flat_workgroup_size: 256
    .name:           _Z8k_layer2PKiS0_PKfS2_PK15HIP_vector_typeIjLj4EES2_Pf
    .private_segment_fixed_size: 0
    .sgpr_count:     52
    .sgpr_spill_count: 0
    .symbol:         _Z8k_layer2PKiS0_PKfS2_PK15HIP_vector_typeIjLj4EES2_Pf.kd
    .uniform_work_group_size: 1
    .uses_dynamic_stack: false
    .vgpr_count:     70
    .vgpr_spill_count: 0
    .wavefront_size: 64
